# v91: v85 + M3 retention norm weights requested once per pass and head (tag register) instead of per item
# speedup vs baseline: 1.0062x; 1.0048x over previous
.LBB0_547:
	s_and_b64 s[4:5], exec, s[96:97]
	s_cselect_b32 s81, s12, 0x200
	s_cmp_ge_i32 s3, s81
	s_cbranch_scc1 .LBB0_561
	s_waitcnt vmcnt(3)
	v_mul_f32_e32 v5, 0x3fb8aa3b, v1
	v_rndne_f32_e32 v6, v5
	s_mov_b32 s4, 0x3fb8aa3b
	v_sub_f32_e32 v7, v5, v6
	v_fma_f32 v5, v1, s4, -v5
	v_fmac_f32_e32 v5, 0x32a5705f, v1
	v_add_f32_e32 v5, v7, v5
	v_exp_f32_e32 v5, v5
	v_cvt_i32_f32_e32 v6, v6
	s_mov_b32 s5, 0xc2ce8ed0
	v_cmp_ngt_f32_e32 vcc, s5, v1
	s_mov_b32 s10, 0x42b17218
	v_ldexp_f32 v5, v5, v6
	v_cndmask_b32_e32 v5, 0, v5, vcc
	v_cmp_nlt_f32_e32 vcc, s10, v1
	s_nop 1
	v_cndmask_b32_e32 v1, v211, v5, vcc
	s_waitcnt vmcnt(2)
	v_mul_f32_e32 v5, 0x3fb8aa3b, v4
	v_rndne_f32_e32 v6, v5
	v_sub_f32_e32 v7, v5, v6
	v_fma_f32 v5, v4, s4, -v5
	v_fmac_f32_e32 v5, 0x32a5705f, v4
	v_add_f32_e32 v5, v7, v5
	v_exp_f32_e32 v5, v5
	v_cvt_i32_f32_e32 v6, v6
	v_cmp_ngt_f32_e32 vcc, s5, v4
	v_ldexp_f32 v5, v5, v6
	s_nop 0
	v_cndmask_b32_e32 v5, 0, v5, vcc
	v_cmp_nlt_f32_e32 vcc, s10, v4
	s_waitcnt vmcnt(1)
	v_mul_f32_e32 v4, 0x3fb8aa3b, v3
	v_cndmask_b32_e32 v141, v211, v5, vcc
	v_rndne_f32_e32 v5, v4
	v_sub_f32_e32 v6, v4, v5
	v_fma_f32 v4, v3, s4, -v4
	v_fmac_f32_e32 v4, 0x32a5705f, v3
	v_add_f32_e32 v4, v6, v4
	v_exp_f32_e32 v4, v4
	v_cvt_i32_f32_e32 v5, v5
	v_cmp_ngt_f32_e32 vcc, s5, v3
	v_ldexp_f32 v4, v4, v5
	s_nop 0
	v_cndmask_b32_e32 v4, 0, v4, vcc
	v_cmp_nlt_f32_e32 vcc, s10, v3
	s_waitcnt vmcnt(0)
	v_mul_f32_e32 v3, 0x3fb8aa3b, v2
	v_cndmask_b32_e32 v142, v211, v4, vcc
	v_rndne_f32_e32 v4, v3
	v_sub_f32_e32 v5, v3, v4
	v_fma_f32 v3, v2, s4, -v3
	v_fmac_f32_e32 v3, 0x32a5705f, v2
	v_add_f32_e32 v3, v5, v3
	v_exp_f32_e32 v3, v3
	v_cvt_i32_f32_e32 v4, v4
	s_or_b32 s4, s2, s17
	v_cmp_ngt_f32_e32 vcc, s5, v2
	s_cmp_eq_u32 s4, 0
	v_ldexp_f32 v3, v3, v4
	v_cndmask_b32_e32 v3, 0, v3, vcc
	v_cmp_nlt_f32_e32 vcc, s10, v2
	s_cselect_b64 s[4:5], -1, 0
	s_and_b64 s[20:21], s[86:87], s[4:5]
	v_cndmask_b32_e32 v143, v211, v3, vcc
	v_mov_b32_e32 v254, -1
	s_branch .LBB0_551

.LBB0_555:
	s_and_b32 s33, s3, 1
	s_lshl_b32 s4, s33, 1
	s_add_i32 s14, s4, s18
	s_mul_i32 s4, s10, 0x1100
	s_lshl_b32 s5, s11, 7
	s_add_i32 s45, s4, s5
	s_lshl_b32 s22, s14, 6
	v_or_b32_e32 v2, s45, v116
	v_mov_b64_e32 v[50:51], s[88:89]
	s_mul_i32 s5, s14, 0x44
	s_ashr_i32 s23, s22, 31
	v_mad_i64_i32 v[2:3], s[14:15], v2, s60, v[50:51]
	s_lshl_b64 s[14:15], s[22:23], 1
	v_mov_b32_e32 v101, v0
	v_lshl_add_u64 v[2:3], v[2:3], 0, s[14:15]
	v_or_b32_e32 v10, s45, v117
	v_lshl_add_u64 v[2:3], v[2:3], 0, v[100:101]
	v_mad_i64_i32 v[10:11], s[26:27], v10, s60, v[50:51]
	s_mul_i32 s4, s10, 0x110
	v_add_co_u32_e32 v6, vcc, s78, v2
	v_lshl_add_u64 v[10:11], v[10:11], 0, s[14:15]
	v_or_b32_e32 v18, s45, v118
	s_add_i32 s4, s4, s5
	v_addc_co_u32_e32 v7, vcc, 0, v3, vcc
	v_lshl_add_u64 v[10:11], v[10:11], 0, v[100:101]
	v_mad_i64_i32 v[18:19], s[26:27], v18, s60, v[50:51]
	s_add_i32 s4, s4, s11
	v_add_co_u32_e32 v14, vcc, s78, v10
	v_lshl_add_u64 v[18:19], v[18:19], 0, s[14:15]
	v_or_b32_e32 v26, s45, v119
	s_ashr_i32 s5, s4, 31
	v_addc_co_u32_e32 v15, vcc, 0, v11, vcc
	v_lshl_add_u64 v[18:19], v[18:19], 0, v[100:101]
	v_mad_i64_i32 v[26:27], s[26:27], v26, s60, v[50:51]
	s_lshl_b64 s[10:11], s[4:5], 13
	s_add_i32 s4, s4, 34
	v_add_co_u32_e32 v22, vcc, s78, v18
	v_lshl_add_u64 v[26:27], v[26:27], 0, s[14:15]
	s_ashr_i32 s5, s4, 31
	v_addc_co_u32_e32 v23, vcc, 0, v19, vcc
	v_lshl_add_u64 v[26:27], v[26:27], 0, v[100:101]
	s_lshl_b64 s[4:5], s[4:5], 13
	v_add_co_u32_e32 v30, vcc, s78, v26
	s_cmp_eq_u32 s33, 0
	s_nop 0
	v_addc_co_u32_e32 v31, vcc, 0, v27, vcc
	s_cselect_b64 vcc, -1, 0
	s_add_u32 s10, s66, s10
	s_addc_u32 s11, s67, s11
	s_add_u32 s4, s66, s4
	s_addc_u32 s5, s67, s5
	v_or_b32_e32 v104, s45, v109
	global_load_dwordx4 v[2:5], v[6:7], off offset:512
	s_nop 0
	global_load_dwordx4 v[6:9], v[6:7], off
	s_nop 0
	global_load_dwordx4 v[10:13], v[14:15], off offset:512
	s_nop 0
	global_load_dwordx4 v[14:17], v[14:15], off
	s_nop 0
	global_load_dwordx4 v[18:21], v[22:23], off offset:512
	s_nop 0
	global_load_dwordx4 v[22:25], v[22:23], off
	s_nop 0
	global_load_dwordx4 v[26:29], v[30:31], off offset:512
	s_nop 0
	global_load_dwordx4 v[30:33], v[30:31], off
	s_nop 0
	global_load_dwordx4 v[34:37], v125, s[10:11]
	global_load_dwordx4 v[38:41], v125, s[4:5]
	global_load_dwordx4 v[42:45], v126, s[10:11]
	global_load_dwordx4 v[46:49], v126, s[4:5]
	v_mad_i64_i32 v[106:107], s[4:5], v104, s60, v[50:51]
	v_lshl_add_u64 v[50:51], v[106:107], 0, s[14:15]
	v_mov_b32_e32 v103, v0
	v_lshl_add_u64 v[50:51], v[50:51], 0, v[102:103]
	global_load_dwordx4 v[78:81], v[50:51], off offset:3584
	global_load_dwordx4 v[74:77], v[50:51], off offset:3616
	global_load_dwordx4 v[70:73], v[50:51], off offset:3648
	global_load_dwordx4 v[66:69], v[50:51], off offset:3680
	v_cndmask_b32_e32 v50, v142, v1, vcc
	s_mov_b32 s10, 0
	v_mul_f32_e32 v101, 0xbfb8aa3b, v50
	v_ashrrev_i32_e32 v105, 31, v104
	s_mov_b64 s[4:5], -1
	s_waitcnt vmcnt(15)
	ds_write_b128 v127, v[2:5]
	s_waitcnt vmcnt(14)
	ds_write_b128 v128, v[6:9] offset:16384
	s_waitcnt vmcnt(13)
	ds_write_b128 v129, v[10:13]
	s_waitcnt vmcnt(12)
	ds_write_b128 v130, v[14:17] offset:16384
	s_waitcnt vmcnt(11)
	ds_write_b128 v127, v[18:21] offset:8192
	s_waitcnt vmcnt(10)
	ds_write_b128 v131, v[22:25] offset:16384
	s_waitcnt vmcnt(9)
	ds_write_b128 v132, v[26:29] offset:8192
	s_waitcnt vmcnt(8)
	ds_write_b128 v133, v[30:33] offset:16384
	s_waitcnt vmcnt(7)
	ds_write_b128 v128, v[34:37] offset:32768
	s_waitcnt vmcnt(6)
	ds_write_b128 v128, v[38:41] offset:40960
	s_waitcnt vmcnt(5)
	ds_write_b128 v130, v[42:45] offset:32768
	s_waitcnt vmcnt(4)
	ds_write_b128 v130, v[46:49] offset:40960
	v_cndmask_b32_e32 v2, v143, v141, vcc
	v_mov_b32_e32 v18, 0
	v_mul_f32_e32 v103, 0xbfb8aa3b, v2
	v_mul_f32_e32 v167, 0xbf800000, v101
	v_mul_f32_e32 v168, 0xc0000000, v101
	v_mul_f32_e32 v169, 0xc0400000, v101
	v_mul_f32_e32 v170, 0xc1000000, v101
	v_mul_f32_e32 v171, 0x3f800000, v103
	v_mul_f32_e32 v172, 0x40000000, v103
	v_mul_f32_e32 v173, 0x40400000, v103
	v_mul_f32_e32 v174, 0x41000000, v103
	v_exp_f32_e32 v167, v167
	v_exp_f32_e32 v168, v168
	v_exp_f32_e32 v169, v169
	v_exp_f32_e32 v170, v170
	v_exp_f32_e32 v171, v171
	v_exp_f32_e32 v172, v172
	v_exp_f32_e32 v173, v173
	v_exp_f32_e32 v174, v174
	v_mov_b32_e32 v19, v18
	v_mov_b32_e32 v20, v18
	v_mov_b32_e32 v21, v18
	v_mov_b32_e32 v22, v18
	v_mov_b32_e32 v23, v18
	v_mov_b32_e32 v24, v18
	v_mov_b32_e32 v25, v18
	v_mov_b32_e32 v26, v18
	v_mov_b32_e32 v27, v18
	v_mov_b32_e32 v28, v18
	v_mov_b32_e32 v29, v18
	v_mov_b32_e32 v30, v18
	v_mov_b32_e32 v31, v18
	v_mov_b32_e32 v32, v18
	v_mov_b32_e32 v33, v18
	v_mov_b32_e32 v2, v18
	v_mov_b32_e32 v3, v18
	v_mov_b32_e32 v4, v18
	v_mov_b32_e32 v5, v18
	v_mov_b32_e32 v6, v18
	v_mov_b32_e32 v7, v18
	v_mov_b32_e32 v8, v18
	v_mov_b32_e32 v9, v18
	v_mov_b32_e32 v10, v18
	v_mov_b32_e32 v11, v18
	v_mov_b32_e32 v12, v18
	v_mov_b32_e32 v13, v18
	v_mov_b32_e32 v14, v18
	v_mov_b32_e32 v15, v18
	v_mov_b32_e32 v16, v18
	v_mov_b32_e32 v17, v18
	s_waitcnt lgkmcnt(0)
	s_barrier
	v_lshl_add_u64 v[152:153], s[22:23], 1, v[106:107]
	v_lshlrev_b32_e32 v154, 1, v82
	v_mov_b32_e32 v155, v0
	v_lshl_add_u64 v[152:153], v[152:153], 0, v[154:155]
	s_mov_b64 s[98:99], 0x1400
	v_lshl_add_u64 v[154:155], v[152:153], 0, s[98:99]
	v_add_co_u32_e32 v152, vcc, s78, v152
	s_nop 1
	v_addc_co_u32_e32 v153, vcc, 0, v153, vcc
	global_load_dwordx2 v[222:223], v[152:153], off offset:1024
	global_load_dwordx2 v[224:225], v[154:155], off offset:16
	global_load_dwordx2 v[226:227], v[154:155], off offset:32
	global_load_dwordx2 v[228:229], v[154:155], off offset:48
	global_load_dwordx2 v[230:231], v[154:155], off offset:64
	global_load_dwordx2 v[232:233], v[154:155], off offset:80
	global_load_dwordx2 v[234:235], v[154:155], off offset:96
	global_load_dwordx2 v[236:237], v[154:155], off offset:112
	v_cmp_eq_u32_e32 vcc, s22, v254
	s_cbranch_vccnz .Lm3r_wcached
	ds_read_b64 v[156:157], v0 offset:640
	s_lshl_b64 s[98:99], s[24:25], 2
	s_lshl_b64 s[100:101], s[22:23], 2
	s_add_u32 s98, s98, s100
	s_addc_u32 s99, s99, s101
	s_waitcnt lgkmcnt(0)
	v_readfirstlane_b32 s100, v156
	v_readfirstlane_b32 s101, v157
	v_lshlrev_b32_e32 v152, 2, v82
	s_add_u32 s98, s100, s98
	s_addc_u32 s99, s101, s99
	global_load_dwordx4 v[238:241], v152, s[98:99]
	global_load_dwordx4 v[242:245], v152, s[98:99] offset:32
	global_load_dwordx4 v[246:249], v152, s[98:99] offset:64
	global_load_dwordx4 v[250:253], v152, s[98:99] offset:96
	global_load_dwordx4 v[200:203], v152, s[98:99] offset:128
	global_load_dwordx4 v[204:207], v152, s[98:99] offset:160
	global_load_dwordx4 v[214:217], v152, s[98:99] offset:192
	global_load_dwordx4 v[192:195], v152, s[98:99] offset:224
	v_mov_b32_e32 v254, s22
.Lm3r_wcached:
.LBB0_556:
	v_cndmask_b32_e64 v34, 0, 1, s[4:5]
	s_lshl_b32 s4, s10, 6
	v_cmp_ne_u32_e32 vcc, 1, v34
	v_or_b32_e32 v34, s4, v108
	v_lshl_add_u32 v152, v34, 7, s58
	v_add_u32_e32 v38, v152, v120
	ds_read_b128 v[34:37], v38 offset:16384
	ds_read_b128 v[50:53], v38 offset:20480
	v_add_u32_e32 v148, v152, v121
	s_waitcnt vmcnt(11) lgkmcnt(1)
	v_mfma_f32_32x32x16_bf16 v[34:49], v[34:37], v[78:81], 0
	ds_read_b128 v[144:147], v148 offset:16384
	ds_read_b128 v[148:151], v148 offset:20480
	s_waitcnt lgkmcnt(2)
	v_mfma_f32_32x32x16_bf16 v[50:65], v[50:53], v[78:81], 0
	s_waitcnt vmcnt(10) lgkmcnt(1)
	v_mfma_f32_32x32x16_bf16 v[34:49], v[144:147], v[74:77], v[34:49]
	s_waitcnt lgkmcnt(0)
	v_mfma_f32_32x32x16_bf16 v[50:65], v[148:151], v[74:77], v[50:65]
	v_add_u32_e32 v148, v152, v122
	ds_read_b128 v[144:147], v148 offset:16384
	ds_read_b128 v[148:151], v148 offset:20480
	s_waitcnt vmcnt(9) lgkmcnt(1)
	v_mfma_f32_32x32x16_bf16 v[34:49], v[144:147], v[70:73], v[34:49]
	s_waitcnt lgkmcnt(0)
	v_mfma_f32_32x32x16_bf16 v[50:65], v[148:151], v[70:73], v[50:65]
	v_add_u32_e32 v148, v152, v123
	ds_read_b128 v[144:147], v148 offset:16384
	ds_read_b128 v[148:151], v148 offset:20480
	s_waitcnt vmcnt(8) lgkmcnt(1)
	v_mfma_f32_32x32x16_bf16 v[34:49], v[144:147], v[66:69], v[34:49]
	v_or_b32_e32 v145, s4, v82
	s_waitcnt lgkmcnt(0)
	v_mfma_f32_32x32x16_bf16 v[50:65], v[148:151], v[66:69], v[50:65]
	v_sub_u32_e32 v166, v109, v145
	v_cvt_f32_i32_e32 v166, v166
	v_mul_f32_e32 v175, v101, v166
	v_mul_f32_e64 v183, -v103, v166
	v_exp_f32_e32 v175, v175
	v_exp_f32_e32 v183, v183
	s_nop 0
	v_mul_f32_e32 v176, v175, v170
	v_mul_f32_e32 v184, v183, v174
	v_mul_f32_e32 v177, v176, v170
	v_mul_f32_e32 v185, v184, v174
	v_mul_f32_e32 v178, v177, v170
	v_mul_f32_e32 v186, v185, v174
	v_mul_f32_e32 v179, v178, v170
	v_mul_f32_e32 v187, v186, v174
	v_mul_f32_e32 v180, v179, v170
	v_mul_f32_e32 v188, v187, v174
	v_mul_f32_e32 v181, v180, v170
	v_mul_f32_e32 v189, v188, v174
	v_mul_f32_e32 v182, v181, v170
	v_mul_f32_e32 v190, v189, v174
	v_min_f32_e32 v160, v175, v183
	v_mul_f32_e32 v144, v34, v160
	v_min_f32_e32 v162, v179, v187
	v_mul_f32_e32 v34, v50, v162
	v_mul_f32_e32 v164, v175, v167
	v_mul_f32_e32 v165, v183, v171
	v_min_f32_e32 v164, v164, v165
	v_mul_f32_e32 v50, v35, v164
	v_mul_f32_e32 v160, v179, v167
	v_mul_f32_e32 v161, v187, v171
	v_min_f32_e32 v160, v160, v161
	v_mul_f32_e32 v35, v51, v160
	v_mul_f32_e32 v162, v175, v168
	v_mul_f32_e32 v163, v183, v172
	v_min_f32_e32 v162, v162, v163
	v_mul_f32_e32 v51, v36, v162
	v_mul_f32_e32 v164, v179, v168
	v_mul_f32_e32 v165, v187, v172
	v_min_f32_e32 v164, v164, v165
	v_mul_f32_e32 v36, v52, v164
	v_mul_f32_e32 v160, v175, v169
	v_mul_f32_e32 v161, v183, v173
	v_min_f32_e32 v160, v160, v161
	v_mul_f32_e32 v52, v37, v160
	v_mul_f32_e32 v162, v179, v169
	v_mul_f32_e32 v163, v187, v173
	v_min_f32_e32 v162, v162, v163
	v_mul_f32_e32 v37, v53, v162
	v_min_f32_e32 v164, v176, v184
	v_mul_f32_e32 v53, v38, v164
	v_min_f32_e32 v160, v180, v188
	v_mul_f32_e32 v38, v54, v160
	v_mul_f32_e32 v162, v176, v167
	v_mul_f32_e32 v163, v184, v171
	v_min_f32_e32 v162, v162, v163
	v_mul_f32_e32 v54, v39, v162
	v_mul_f32_e32 v164, v180, v167
	v_mul_f32_e32 v165, v188, v171
	v_min_f32_e32 v164, v164, v165
	v_mul_f32_e32 v39, v55, v164
	v_mul_f32_e32 v160, v176, v168
	v_mul_f32_e32 v161, v184, v172
	v_min_f32_e32 v160, v160, v161
	v_mul_f32_e32 v55, v40, v160
	v_mul_f32_e32 v162, v180, v168
	v_mul_f32_e32 v163, v188, v172
	v_min_f32_e32 v162, v162, v163
	v_mul_f32_e32 v40, v56, v162
	v_mul_f32_e32 v164, v176, v169
	v_mul_f32_e32 v165, v184, v173
	v_min_f32_e32 v164, v164, v165
	v_mul_f32_e32 v56, v41, v164
	v_mul_f32_e32 v160, v180, v169
	v_mul_f32_e32 v161, v188, v173
	v_min_f32_e32 v160, v160, v161
	v_mul_f32_e32 v41, v57, v160
	v_min_f32_e32 v162, v177, v185
	v_mul_f32_e32 v57, v42, v162
	v_min_f32_e32 v164, v181, v189
	v_mul_f32_e32 v42, v58, v164
	v_mul_f32_e32 v160, v177, v167
	v_mul_f32_e32 v161, v185, v171
	v_min_f32_e32 v160, v160, v161
	v_mul_f32_e32 v43, v43, v160
	v_mul_f32_e32 v162, v181, v167
	v_mul_f32_e32 v163, v189, v171
	v_min_f32_e32 v162, v162, v163
	v_mul_f32_e32 v58, v59, v162
	v_mul_f32_e32 v164, v177, v168
	v_mul_f32_e32 v165, v185, v172
	v_min_f32_e32 v164, v164, v165
	v_mul_f32_e32 v59, v44, v164
	v_mul_f32_e32 v160, v181, v168
	v_mul_f32_e32 v161, v189, v172
	v_min_f32_e32 v160, v160, v161
	v_mul_f32_e32 v60, v60, v160
	v_mul_f32_e32 v162, v177, v169
	v_mul_f32_e32 v163, v185, v173
	v_min_f32_e32 v162, v162, v163
	v_mul_f32_e32 v147, v45, v162
	v_mul_f32_e32 v164, v181, v169
	v_mul_f32_e32 v165, v189, v173
	v_min_f32_e32 v164, v164, v165
	v_mul_f32_e32 v61, v61, v164
	v_min_f32_e32 v160, v178, v186
	v_mul_f32_e32 v146, v46, v160
	v_min_f32_e32 v162, v182, v190
	v_mul_f32_e32 v62, v62, v162
	v_mul_f32_e32 v164, v178, v167
	v_mul_f32_e32 v165, v186, v171
	v_min_f32_e32 v164, v164, v165
	v_mul_f32_e32 v148, v47, v164
	v_mul_f32_e32 v160, v182, v167
	v_mul_f32_e32 v161, v190, v171
	v_min_f32_e32 v160, v160, v161
	v_mul_f32_e32 v63, v63, v160
	v_mul_f32_e32 v162, v178, v168
	v_mul_f32_e32 v163, v186, v172
	v_min_f32_e32 v162, v162, v163
	v_mul_f32_e32 v149, v48, v162
	v_mul_f32_e32 v164, v182, v168
	v_mul_f32_e32 v165, v190, v172
	v_min_f32_e32 v164, v164, v165
	v_mul_f32_e32 v64, v64, v164
	v_mul_f32_e32 v160, v178, v169
	v_mul_f32_e32 v161, v186, v173
	v_min_f32_e32 v160, v160, v161
	v_mul_f32_e32 v145, v49, v160
	v_mul_f32_e32 v162, v182, v169
	v_mul_f32_e32 v163, v190, v173
	v_min_f32_e32 v162, v162, v163
	v_mul_f32_e32 v65, v65, v162
	v_cvt_pk_bf16_f32 v44, v144, v50
	v_cvt_pk_bf16_f32 v45, v51, v52
	v_cvt_pk_bf16_f32 v46, v53, v54
	v_cvt_pk_bf16_f32 v47, v55, v56
	v_cvt_pk_bf16_f32 v48, v57, v43
	v_cvt_pk_bf16_f32 v49, v59, v147
	v_cvt_pk_bf16_f32 v50, v146, v148
	v_cvt_pk_bf16_f32 v51, v149, v145
	v_cvt_pk_bf16_f32 v34, v34, v35
	v_cvt_pk_bf16_f32 v35, v36, v37
	v_cvt_pk_bf16_f32 v36, v38, v39
	v_cvt_pk_bf16_f32 v37, v40, v41
	v_cvt_pk_bf16_f32 v38, v42, v58
	v_cvt_pk_bf16_f32 v39, v60, v61
	v_cvt_pk_bf16_f32 v40, v62, v63
	v_cvt_pk_bf16_f32 v41, v64, v65
	v_lshl_add_u32 v42, s10, 13, v110
	ds_read_b64_tr_b16 v[52:53], v42 offset:0
	ds_read_b64_tr_b16 v[54:55], v42 offset:0x400
	ds_read_b64_tr_b16 v[56:57], v42 offset:0x800
	ds_read_b64_tr_b16 v[58:59], v42 offset:0xc00
	ds_read_b64_tr_b16 v[60:61], v42 offset:0x1000
	ds_read_b64_tr_b16 v[62:63], v42 offset:0x1400
	ds_read_b64_tr_b16 v[144:145], v42 offset:0x1800
	ds_read_b64_tr_b16 v[146:147], v42 offset:0x1c00
	s_waitcnt lgkmcnt(0)
	v_permlane32_swap_b32_e32 v44, v46
	v_permlane32_swap_b32_e32 v45, v47
	v_permlane32_swap_b32_e32 v48, v50
	v_permlane32_swap_b32_e32 v49, v51
	v_permlane32_swap_b32_e32 v34, v36
	v_permlane32_swap_b32_e32 v35, v37
	v_permlane32_swap_b32_e32 v38, v40
	v_permlane32_swap_b32_e32 v39, v41
	v_mfma_f32_32x32x16_bf16 v[18:33], v[52:55], v[44:47], v[18:33]
	ds_read_b64_tr_b16 v[52:53], v42 offset:0x200
	ds_read_b64_tr_b16 v[54:55], v42 offset:0x600
	v_mfma_f32_32x32x16_bf16 v[18:33], v[56:59], v[48:51], v[18:33]
	ds_read_b64_tr_b16 v[56:57], v42 offset:0xa00
	ds_read_b64_tr_b16 v[58:59], v42 offset:0xe00
	v_mfma_f32_32x32x16_bf16 v[18:33], v[60:63], v[34:37], v[18:33]
	ds_read_b64_tr_b16 v[60:61], v42 offset:0x1200
	ds_read_b64_tr_b16 v[62:63], v42 offset:0x1600
	v_mfma_f32_32x32x16_bf16 v[18:33], v[144:147], v[38:41], v[18:33]
	ds_read_b64_tr_b16 v[144:145], v42 offset:0x1a00
	ds_read_b64_tr_b16 v[146:147], v42 offset:0x1e00
	s_waitcnt lgkmcnt(0)
	v_mfma_f32_32x32x16_bf16 v[2:17], v[52:55], v[44:47], v[2:17]
	s_mov_b64 s[4:5], 0
	s_and_b64 vcc, exec, vcc
	s_mov_b32 s10, 1
	v_mfma_f32_32x32x16_bf16 v[2:17], v[56:59], v[48:51], v[2:17]
	v_mfma_f32_32x32x16_bf16 v[2:17], v[60:63], v[34:37], v[2:17]
	v_mfma_f32_32x32x16_bf16 v[2:17], v[144:147], v[38:41], v[2:17]
	s_cbranch_vccz .LBB0_556
	v_mul_f32_e32 v34, v101, v111
	v_exp_f32_e32 v50, v34
	v_mul_f32_e32 v34, v103, v112
	v_exp_f32_e32 v51, v34
	v_lshlrev_b32_e32 v35, 16, v78
	v_and_b32_e32 v36, 0xffff0000, v78
	v_mul_f32_e32 v34, v50, v35
	v_mul_f32_e32 v37, v50, v36
	v_mul_f32_e32 v36, v51, v36
	v_cvt_pk_bf16_f32 v34, v34, v37
	v_mul_f32_e32 v35, v51, v35
	v_cvt_pk_bf16_f32 v38, v35, v36
	v_lshlrev_b32_e32 v36, 16, v79
	v_and_b32_e32 v37, 0xffff0000, v79
	v_mul_f32_e32 v35, v50, v36
	v_mul_f32_e32 v39, v50, v37
	v_mul_f32_e32 v37, v51, v37
	v_cvt_pk_bf16_f32 v35, v35, v39
	v_mul_f32_e32 v36, v51, v36
	v_cvt_pk_bf16_f32 v39, v36, v37
	v_lshlrev_b32_e32 v37, 16, v80
	v_and_b32_e32 v40, 0xffff0000, v80
	v_mul_f32_e32 v36, v50, v37
	v_mul_f32_e32 v41, v50, v40
	v_cvt_pk_bf16_f32 v36, v36, v41
	v_mul_f32_e32 v37, v51, v37
	v_mul_f32_e32 v40, v51, v40
	v_lshlrev_b32_e32 v41, 16, v81
	v_and_b32_e32 v42, 0xffff0000, v81
	v_cvt_pk_bf16_f32 v40, v37, v40
	v_mul_f32_e32 v37, v50, v41
	v_mul_f32_e32 v43, v50, v42
	v_mul_f32_e32 v41, v51, v41
	v_mul_f32_e32 v42, v51, v42
	v_cvt_pk_bf16_f32 v37, v37, v43
	v_cvt_pk_bf16_f32 v41, v41, v42
	ds_read_b128 v[42:45], v134 offset:32768
	ds_read_b128 v[46:49], v134 offset:40960
	s_waitcnt lgkmcnt(1)
	v_mfma_f32_32x32x16_bf16 v[18:33], v[42:45], v[34:37], v[18:33]
	s_mov_b64 s[4:5], 0x1400
	s_waitcnt lgkmcnt(0)
	v_mfma_f32_32x32x16_bf16 v[18:33], v[46:49], v[38:41], v[18:33]
	ds_read_b128 v[42:45], v134 offset:36864
	ds_read_b128 v[46:49], v134 offset:45056
	s_waitcnt lgkmcnt(1)
	v_mfma_f32_32x32x16_bf16 v[2:17], v[42:45], v[34:37], v[2:17]
	v_lshlrev_b32_e32 v35, 16, v74
	v_and_b32_e32 v36, 0xffff0000, v74
	v_mul_f32_e32 v34, v50, v35
	v_mul_f32_e32 v37, v50, v36
	v_mul_f32_e32 v36, v51, v36
	v_cvt_pk_bf16_f32 v34, v34, v37
	v_mul_f32_e32 v35, v51, v35
	s_waitcnt lgkmcnt(0)
	v_mfma_f32_32x32x16_bf16 v[2:17], v[46:49], v[38:41], v[2:17]
	v_cvt_pk_bf16_f32 v38, v35, v36
	v_lshlrev_b32_e32 v36, 16, v75
	v_and_b32_e32 v37, 0xffff0000, v75
	v_mul_f32_e32 v35, v50, v36
	v_mul_f32_e32 v39, v50, v37
	v_mul_f32_e32 v37, v51, v37
	v_cvt_pk_bf16_f32 v35, v35, v39
	v_mul_f32_e32 v36, v51, v36
	v_cvt_pk_bf16_f32 v39, v36, v37
	v_lshlrev_b32_e32 v37, 16, v76
	v_and_b32_e32 v40, 0xffff0000, v76
	v_mul_f32_e32 v36, v50, v37
	v_mul_f32_e32 v41, v50, v40
	v_cvt_pk_bf16_f32 v36, v36, v41
	v_mul_f32_e32 v37, v51, v37
	v_mul_f32_e32 v40, v51, v40
	v_lshlrev_b32_e32 v41, 16, v77
	v_and_b32_e32 v42, 0xffff0000, v77
	v_cvt_pk_bf16_f32 v40, v37, v40
	v_mul_f32_e32 v37, v50, v41
	v_mul_f32_e32 v43, v50, v42
	v_mul_f32_e32 v41, v51, v41
	v_mul_f32_e32 v42, v51, v42
	v_cvt_pk_bf16_f32 v37, v37, v43
	v_cvt_pk_bf16_f32 v41, v41, v42
	ds_read_b128 v[42:45], v135 offset:32768
	ds_read_b128 v[46:49], v135 offset:40960
	s_waitcnt lgkmcnt(1)
	v_mfma_f32_32x32x16_bf16 v[18:33], v[42:45], v[34:37], v[18:33]
	s_waitcnt lgkmcnt(0)
	v_mfma_f32_32x32x16_bf16 v[18:33], v[46:49], v[38:41], v[18:33]
	ds_read_b128 v[42:45], v135 offset:36864
	ds_read_b128 v[46:49], v135 offset:45056
	s_waitcnt lgkmcnt(1)
	v_mfma_f32_32x32x16_bf16 v[2:17], v[42:45], v[34:37], v[2:17]
	v_lshlrev_b32_e32 v35, 16, v70
	v_and_b32_e32 v36, 0xffff0000, v70
	v_mul_f32_e32 v34, v50, v35
	v_mul_f32_e32 v37, v50, v36
	v_mul_f32_e32 v36, v51, v36
	v_cvt_pk_bf16_f32 v34, v34, v37
	v_mul_f32_e32 v35, v51, v35
	s_waitcnt lgkmcnt(0)
	v_mfma_f32_32x32x16_bf16 v[2:17], v[46:49], v[38:41], v[2:17]
	v_cvt_pk_bf16_f32 v38, v35, v36
	v_lshlrev_b32_e32 v36, 16, v71
	v_and_b32_e32 v37, 0xffff0000, v71
	v_mul_f32_e32 v35, v50, v36
	v_mul_f32_e32 v39, v50, v37
	v_mul_f32_e32 v37, v51, v37
	v_cvt_pk_bf16_f32 v35, v35, v39
	v_mul_f32_e32 v36, v51, v36
	v_cvt_pk_bf16_f32 v39, v36, v37
	v_lshlrev_b32_e32 v37, 16, v72
	v_and_b32_e32 v40, 0xffff0000, v72
	v_mul_f32_e32 v36, v50, v37
	v_mul_f32_e32 v41, v50, v40
	v_cvt_pk_bf16_f32 v36, v36, v41
	v_mul_f32_e32 v37, v51, v37
	v_mul_f32_e32 v40, v51, v40
	v_lshlrev_b32_e32 v41, 16, v73
	v_and_b32_e32 v42, 0xffff0000, v73
	v_cvt_pk_bf16_f32 v40, v37, v40
	v_mul_f32_e32 v37, v50, v41
	v_mul_f32_e32 v43, v50, v42
	v_mul_f32_e32 v41, v51, v41
	v_mul_f32_e32 v42, v51, v42
	v_cvt_pk_bf16_f32 v37, v37, v43
	v_cvt_pk_bf16_f32 v41, v41, v42
	ds_read_b128 v[42:45], v136 offset:32768
	ds_read_b128 v[46:49], v136 offset:40960
	s_waitcnt lgkmcnt(1)
	v_mfma_f32_32x32x16_bf16 v[18:33], v[42:45], v[34:37], v[18:33]
	s_waitcnt lgkmcnt(0)
	v_mfma_f32_32x32x16_bf16 v[18:33], v[46:49], v[38:41], v[18:33]
	ds_read_b128 v[42:45], v136 offset:36864
	ds_read_b128 v[46:49], v136 offset:45056
	s_waitcnt lgkmcnt(1)
	v_mfma_f32_32x32x16_bf16 v[2:17], v[42:45], v[34:37], v[2:17]
	v_lshlrev_b32_e32 v35, 16, v66
	v_and_b32_e32 v36, 0xffff0000, v66
	v_mul_f32_e32 v34, v50, v35
	v_mul_f32_e32 v37, v50, v36
	v_mul_f32_e32 v36, v51, v36
	v_cvt_pk_bf16_f32 v34, v34, v37
	v_mul_f32_e32 v35, v51, v35
	s_waitcnt lgkmcnt(0)
	v_mfma_f32_32x32x16_bf16 v[2:17], v[46:49], v[38:41], v[2:17]
	v_cvt_pk_bf16_f32 v38, v35, v36
	v_lshlrev_b32_e32 v36, 16, v67
	v_and_b32_e32 v37, 0xffff0000, v67
	v_mul_f32_e32 v35, v50, v36
	v_mul_f32_e32 v39, v50, v37
	v_mul_f32_e32 v37, v51, v37
	v_cvt_pk_bf16_f32 v35, v35, v39
	v_mul_f32_e32 v36, v51, v36
	v_cvt_pk_bf16_f32 v39, v36, v37
	v_lshlrev_b32_e32 v37, 16, v68
	v_and_b32_e32 v40, 0xffff0000, v68
	v_mul_f32_e32 v36, v50, v37
	v_mul_f32_e32 v41, v50, v40
	v_cvt_pk_bf16_f32 v36, v36, v41
	v_mul_f32_e32 v37, v51, v37
	v_mul_f32_e32 v40, v51, v40
	v_lshlrev_b32_e32 v41, 16, v69
	v_and_b32_e32 v42, 0xffff0000, v69
	v_cvt_pk_bf16_f32 v40, v37, v40
	v_mul_f32_e32 v37, v50, v41
	v_mul_f32_e32 v43, v50, v42
	v_mul_f32_e32 v41, v51, v41
	v_mul_f32_e32 v42, v51, v42
	v_cvt_pk_bf16_f32 v37, v37, v43
	v_cvt_pk_bf16_f32 v41, v41, v42
	ds_read_b128 v[42:45], v137 offset:32768
	ds_read_b128 v[46:49], v137 offset:40960
	s_waitcnt lgkmcnt(1)
	v_mfma_f32_32x32x16_bf16 v[18:33], v[42:45], v[34:37], v[18:33]
	s_waitcnt lgkmcnt(0)
	v_mfma_f32_32x32x16_bf16 v[18:33], v[46:49], v[38:41], v[18:33]
	ds_read_b128 v[42:45], v137 offset:36864
	ds_read_b128 v[46:49], v137 offset:45056
	s_waitcnt lgkmcnt(1)
	v_mfma_f32_32x32x16_bf16 v[2:17], v[42:45], v[34:37], v[2:17]
	s_waitcnt lgkmcnt(0)
	v_mfma_f32_32x32x16_bf16 v[2:17], v[46:49], v[38:41], v[2:17]
	s_nop 7
	v_mul_f32_e32 v78, v19, v19
	v_fmac_f32_e32 v78, v18, v18
	v_fmac_f32_e32 v78, v20, v20
	v_fmac_f32_e32 v78, v21, v21
	v_fmac_f32_e32 v78, v22, v22
	v_fmac_f32_e32 v78, v23, v23
	v_fmac_f32_e32 v78, v24, v24
	v_fmac_f32_e32 v78, v25, v25
	v_fmac_f32_e32 v78, v26, v26
	v_fmac_f32_e32 v78, v27, v27
	v_fmac_f32_e32 v78, v28, v28
	v_fmac_f32_e32 v78, v29, v29
	v_fmac_f32_e32 v78, v30, v30
	v_fmac_f32_e32 v78, v31, v31
	v_fmac_f32_e32 v78, v32, v32
	v_fmac_f32_e32 v78, v33, v33
	v_fmac_f32_e32 v78, v2, v2
	v_fmac_f32_e32 v78, v3, v3
	v_fmac_f32_e32 v78, v4, v4
	v_fmac_f32_e32 v78, v5, v5
	v_fmac_f32_e32 v78, v6, v6
	v_fmac_f32_e32 v78, v7, v7
	v_fmac_f32_e32 v78, v8, v8
	v_fmac_f32_e32 v78, v9, v9
	v_fmac_f32_e32 v78, v10, v10
	v_fmac_f32_e32 v78, v11, v11
	v_fmac_f32_e32 v78, v12, v12
	v_fmac_f32_e32 v78, v13, v13
	v_fmac_f32_e32 v78, v14, v14
	v_fmac_f32_e32 v78, v15, v15
	v_pk_mul_f32 v[62:63], v[16:17], v[16:17]
	s_and_b64 vcc, exec, s[20:21]
	v_add_f32_e32 v62, v78, v62
	v_add_f32_e32 v62, v62, v63
	v_mov_b32_e32 v63, v62
	s_nop 1
	v_permlane32_swap_b32_e32 v62, v63
	v_add_f32_e32 v62, v62, v63
	v_fmamk_f32 v62, v62, 0x3c800000, v210
	v_rsq_f32_e32 v78, v62
	v_lshlrev_b64 v[62:63], 10, v[104:105]
	v_lshl_add_u64 v[62:63], s[82:83], 0, v[62:63]
	v_lshl_add_u64 v[62:63], v[62:63], 0, s[22:23]
	v_mul_f32_e32 v78, 0x41800000, v78
	v_lshl_add_u64 v[62:63], v[62:63], 0, v[84:85]
	v_rcp_f32_e32 v152, v78
	s_waitcnt vmcnt(7)
	v_lshlrev_b32_e32 v153, 16, v222
	v_and_b32_e32 v154, 0xffff0000, v222
	v_lshlrev_b32_e32 v155, 16, v223
	v_and_b32_e32 v156, 0xffff0000, v223
	v_mul_f32_e32 v157, 0xbfb8aa3b, v153
	v_mul_f32_e32 v158, 0xbfb8aa3b, v154
	v_mul_f32_e32 v159, 0xbfb8aa3b, v155
	v_mul_f32_e32 v160, 0xbfb8aa3b, v156
	v_exp_f32_e32 v157, v157
	v_exp_f32_e32 v158, v158
	v_exp_f32_e32 v159, v159
	v_exp_f32_e32 v160, v160
	v_mul_f32_e32 v161, v18, v238
	v_mul_f32_e32 v162, v19, v239
	v_mul_f32_e32 v163, v20, v240
	v_mul_f32_e32 v164, v21, v241
	v_fma_f32 v157, v157, v152, v152
	v_fma_f32 v158, v158, v152, v152
	v_fma_f32 v159, v159, v152, v152
	v_fma_f32 v160, v160, v152, v152
	v_rcp_f32_e32 v157, v157
	v_rcp_f32_e32 v158, v158
	v_rcp_f32_e32 v159, v159
	v_rcp_f32_e32 v160, v160
	v_mul_f32_e32 v153, v153, v157
	v_mul_f32_e32 v154, v154, v158
	v_mul_f32_e32 v155, v155, v159
	v_mul_f32_e32 v156, v156, v160
	v_mul_f32_e32 v161, v161, v153
	v_mul_f32_e32 v162, v162, v154
	v_mul_f32_e32 v163, v163, v155
	v_mul_f32_e32 v164, v164, v156
	v_cvt_pk_fp8_f32 v18, v161, v162
	v_cvt_pk_fp8_f32 v18, v163, v164 op_sel:[0,0,1]
	s_waitcnt vmcnt(6)
	v_lshlrev_b32_e32 v165, 16, v224
	v_and_b32_e32 v166, 0xffff0000, v224
	v_lshlrev_b32_e32 v167, 16, v225
	v_and_b32_e32 v168, 0xffff0000, v225
	v_mul_f32_e32 v169, 0xbfb8aa3b, v165
	v_mul_f32_e32 v170, 0xbfb8aa3b, v166
	v_mul_f32_e32 v171, 0xbfb8aa3b, v167
	v_mul_f32_e32 v172, 0xbfb8aa3b, v168
	v_exp_f32_e32 v169, v169
	v_exp_f32_e32 v170, v170
	v_exp_f32_e32 v171, v171
	v_exp_f32_e32 v172, v172
	v_mul_f32_e32 v173, v22, v242
	v_mul_f32_e32 v174, v23, v243
	v_mul_f32_e32 v175, v24, v244
	v_mul_f32_e32 v176, v25, v245
	v_fma_f32 v169, v169, v152, v152
	v_fma_f32 v170, v170, v152, v152
	v_fma_f32 v171, v171, v152, v152
	v_fma_f32 v172, v172, v152, v152
	v_rcp_f32_e32 v169, v169
	v_rcp_f32_e32 v170, v170
	v_rcp_f32_e32 v171, v171
	v_rcp_f32_e32 v172, v172
	v_mul_f32_e32 v165, v165, v169
	v_mul_f32_e32 v166, v166, v170
	v_mul_f32_e32 v167, v167, v171
	v_mul_f32_e32 v168, v168, v172
	v_mul_f32_e32 v173, v173, v165
	v_mul_f32_e32 v174, v174, v166
	v_mul_f32_e32 v175, v175, v167
	v_mul_f32_e32 v176, v176, v168
	v_cvt_pk_fp8_f32 v20, v173, v174
	v_cvt_pk_fp8_f32 v20, v175, v176 op_sel:[0,0,1]
	s_waitcnt vmcnt(5)
	v_lshlrev_b32_e32 v153, 16, v226
	v_and_b32_e32 v154, 0xffff0000, v226
	v_lshlrev_b32_e32 v155, 16, v227
	v_and_b32_e32 v156, 0xffff0000, v227
	v_mul_f32_e32 v157, 0xbfb8aa3b, v153
	v_mul_f32_e32 v158, 0xbfb8aa3b, v154
	v_mul_f32_e32 v159, 0xbfb8aa3b, v155
	v_mul_f32_e32 v160, 0xbfb8aa3b, v156
	v_exp_f32_e32 v157, v157
	v_exp_f32_e32 v158, v158
	v_exp_f32_e32 v159, v159
	v_exp_f32_e32 v160, v160
	v_mul_f32_e32 v161, v26, v246
	v_mul_f32_e32 v162, v27, v247
	v_mul_f32_e32 v163, v28, v248
	v_mul_f32_e32 v164, v29, v249
	v_fma_f32 v157, v157, v152, v152
	v_fma_f32 v158, v158, v152, v152
	v_fma_f32 v159, v159, v152, v152
	v_fma_f32 v160, v160, v152, v152
	v_rcp_f32_e32 v157, v157
	v_rcp_f32_e32 v158, v158
	v_rcp_f32_e32 v159, v159
	v_rcp_f32_e32 v160, v160
	v_mul_f32_e32 v153, v153, v157
	v_mul_f32_e32 v154, v154, v158
	v_mul_f32_e32 v155, v155, v159
	v_mul_f32_e32 v156, v156, v160
	v_mul_f32_e32 v161, v161, v153
	v_mul_f32_e32 v162, v162, v154
	v_mul_f32_e32 v163, v163, v155
	v_mul_f32_e32 v164, v164, v156
	v_cvt_pk_fp8_f32 v19, v161, v162
	v_cvt_pk_fp8_f32 v19, v163, v164 op_sel:[0,0,1]
	s_waitcnt vmcnt(4)
	v_lshlrev_b32_e32 v165, 16, v228
	v_and_b32_e32 v166, 0xffff0000, v228
	v_lshlrev_b32_e32 v167, 16, v229
	v_and_b32_e32 v168, 0xffff0000, v229
	v_mul_f32_e32 v169, 0xbfb8aa3b, v165
	v_mul_f32_e32 v170, 0xbfb8aa3b, v166
	v_mul_f32_e32 v171, 0xbfb8aa3b, v167
	v_mul_f32_e32 v172, 0xbfb8aa3b, v168
	v_exp_f32_e32 v169, v169
	v_exp_f32_e32 v170, v170
	v_exp_f32_e32 v171, v171
	v_exp_f32_e32 v172, v172
	v_mul_f32_e32 v173, v30, v250
	v_mul_f32_e32 v174, v31, v251
	v_mul_f32_e32 v175, v32, v252
	v_mul_f32_e32 v176, v33, v253
	v_fma_f32 v169, v169, v152, v152
	v_fma_f32 v170, v170, v152, v152
	v_fma_f32 v171, v171, v152, v152
	v_fma_f32 v172, v172, v152, v152
	v_rcp_f32_e32 v169, v169
	v_rcp_f32_e32 v170, v170
	v_rcp_f32_e32 v171, v171
	v_rcp_f32_e32 v172, v172
	v_mul_f32_e32 v165, v165, v169
	v_mul_f32_e32 v166, v166, v170
	v_mul_f32_e32 v167, v167, v171
	v_mul_f32_e32 v168, v168, v172
	v_mul_f32_e32 v173, v173, v165
	v_mul_f32_e32 v174, v174, v166
	v_mul_f32_e32 v175, v175, v167
	v_mul_f32_e32 v176, v176, v168
	v_cvt_pk_fp8_f32 v21, v173, v174
	v_cvt_pk_fp8_f32 v21, v175, v176 op_sel:[0,0,1]
	v_permlane32_swap_b32_e32 v18, v19
	s_nop 0
	v_permlane32_swap_b32_e32 v20, v21
	global_store_dwordx4 v[62:63], v[18:21], off offset:768
	s_waitcnt vmcnt(4)
	v_lshlrev_b32_e32 v153, 16, v230
	v_and_b32_e32 v154, 0xffff0000, v230
	v_lshlrev_b32_e32 v155, 16, v231
	v_and_b32_e32 v156, 0xffff0000, v231
	v_mul_f32_e32 v157, 0xbfb8aa3b, v153
	v_mul_f32_e32 v158, 0xbfb8aa3b, v154
	v_mul_f32_e32 v159, 0xbfb8aa3b, v155
	v_mul_f32_e32 v160, 0xbfb8aa3b, v156
	v_exp_f32_e32 v157, v157
	v_exp_f32_e32 v158, v158
	v_exp_f32_e32 v159, v159
	v_exp_f32_e32 v160, v160
	v_mul_f32_e32 v161, v2, v200
	v_mul_f32_e32 v162, v3, v201
	v_mul_f32_e32 v163, v4, v202
	v_mul_f32_e32 v164, v5, v203
	v_fma_f32 v157, v157, v152, v152
	v_fma_f32 v158, v158, v152, v152
	v_fma_f32 v159, v159, v152, v152
	v_fma_f32 v160, v160, v152, v152
	v_rcp_f32_e32 v157, v157
	v_rcp_f32_e32 v158, v158
	v_rcp_f32_e32 v159, v159
	v_rcp_f32_e32 v160, v160
	v_mul_f32_e32 v153, v153, v157
	v_mul_f32_e32 v154, v154, v158
	v_mul_f32_e32 v155, v155, v159
	v_mul_f32_e32 v156, v156, v160
	v_mul_f32_e32 v161, v161, v153
	v_mul_f32_e32 v162, v162, v154
	v_mul_f32_e32 v163, v163, v155
	v_mul_f32_e32 v164, v164, v156
	v_cvt_pk_fp8_f32 v2, v161, v162
	v_cvt_pk_fp8_f32 v2, v163, v164 op_sel:[0,0,1]
	s_waitcnt vmcnt(3)
	v_lshlrev_b32_e32 v165, 16, v232
	v_and_b32_e32 v166, 0xffff0000, v232
	v_lshlrev_b32_e32 v167, 16, v233
	v_and_b32_e32 v168, 0xffff0000, v233
	v_mul_f32_e32 v169, 0xbfb8aa3b, v165
	v_mul_f32_e32 v170, 0xbfb8aa3b, v166
	v_mul_f32_e32 v171, 0xbfb8aa3b, v167
	v_mul_f32_e32 v172, 0xbfb8aa3b, v168
	v_exp_f32_e32 v169, v169
	v_exp_f32_e32 v170, v170
	v_exp_f32_e32 v171, v171
	v_exp_f32_e32 v172, v172
	v_mul_f32_e32 v173, v6, v204
	v_mul_f32_e32 v174, v7, v205
	v_mul_f32_e32 v175, v8, v206
	v_mul_f32_e32 v176, v9, v207
	v_fma_f32 v169, v169, v152, v152
	v_fma_f32 v170, v170, v152, v152
	v_fma_f32 v171, v171, v152, v152
	v_fma_f32 v172, v172, v152, v152
	v_rcp_f32_e32 v169, v169
	v_rcp_f32_e32 v170, v170
	v_rcp_f32_e32 v171, v171
	v_rcp_f32_e32 v172, v172
	v_mul_f32_e32 v165, v165, v169
	v_mul_f32_e32 v166, v166, v170
	v_mul_f32_e32 v167, v167, v171
	v_mul_f32_e32 v168, v168, v172
	v_mul_f32_e32 v173, v173, v165
	v_mul_f32_e32 v174, v174, v166
	v_mul_f32_e32 v175, v175, v167
	v_mul_f32_e32 v176, v176, v168
	v_cvt_pk_fp8_f32 v4, v173, v174
	v_cvt_pk_fp8_f32 v4, v175, v176 op_sel:[0,0,1]
	s_waitcnt vmcnt(2)
	v_lshlrev_b32_e32 v153, 16, v234
	v_and_b32_e32 v154, 0xffff0000, v234
	v_lshlrev_b32_e32 v155, 16, v235
	v_and_b32_e32 v156, 0xffff0000, v235
	v_mul_f32_e32 v157, 0xbfb8aa3b, v153
	v_mul_f32_e32 v158, 0xbfb8aa3b, v154
	v_mul_f32_e32 v159, 0xbfb8aa3b, v155
	v_mul_f32_e32 v160, 0xbfb8aa3b, v156
	v_exp_f32_e32 v157, v157
	v_exp_f32_e32 v158, v158
	v_exp_f32_e32 v159, v159
	v_exp_f32_e32 v160, v160
	v_mul_f32_e32 v161, v10, v214
	v_mul_f32_e32 v162, v11, v215
	v_mul_f32_e32 v163, v12, v216
	v_mul_f32_e32 v164, v13, v217
	v_fma_f32 v157, v157, v152, v152
	v_fma_f32 v158, v158, v152, v152
	v_fma_f32 v159, v159, v152, v152
	v_fma_f32 v160, v160, v152, v152
	v_rcp_f32_e32 v157, v157
	v_rcp_f32_e32 v158, v158
	v_rcp_f32_e32 v159, v159
	v_rcp_f32_e32 v160, v160
	v_mul_f32_e32 v153, v153, v157
	v_mul_f32_e32 v154, v154, v158
	v_mul_f32_e32 v155, v155, v159
	v_mul_f32_e32 v156, v156, v160
	v_mul_f32_e32 v161, v161, v153
	v_mul_f32_e32 v162, v162, v154
	v_mul_f32_e32 v163, v163, v155
	v_mul_f32_e32 v164, v164, v156
	v_cvt_pk_fp8_f32 v3, v161, v162
	v_cvt_pk_fp8_f32 v3, v163, v164 op_sel:[0,0,1]
	s_waitcnt vmcnt(1)
	v_lshlrev_b32_e32 v165, 16, v236
	v_and_b32_e32 v166, 0xffff0000, v236
	v_lshlrev_b32_e32 v167, 16, v237
	v_and_b32_e32 v168, 0xffff0000, v237
	v_mul_f32_e32 v169, 0xbfb8aa3b, v165
	v_mul_f32_e32 v170, 0xbfb8aa3b, v166
	v_mul_f32_e32 v171, 0xbfb8aa3b, v167
	v_mul_f32_e32 v172, 0xbfb8aa3b, v168
	v_exp_f32_e32 v169, v169
	v_exp_f32_e32 v170, v170
	v_exp_f32_e32 v171, v171
	v_exp_f32_e32 v172, v172
	v_mul_f32_e32 v173, v14, v192
	v_mul_f32_e32 v174, v15, v193
	v_mul_f32_e32 v175, v16, v194
	v_mul_f32_e32 v176, v17, v195
	v_fma_f32 v169, v169, v152, v152
	v_fma_f32 v170, v170, v152, v152
	v_fma_f32 v171, v171, v152, v152
	v_fma_f32 v172, v172, v152, v152
	v_rcp_f32_e32 v169, v169
	v_rcp_f32_e32 v170, v170
	v_rcp_f32_e32 v171, v171
	v_rcp_f32_e32 v172, v172
	v_mul_f32_e32 v165, v165, v169
	v_mul_f32_e32 v166, v166, v170
	v_mul_f32_e32 v167, v167, v171
	v_mul_f32_e32 v168, v168, v172
	v_mul_f32_e32 v173, v173, v165
	v_mul_f32_e32 v174, v174, v166
	v_mul_f32_e32 v175, v175, v167
	v_mul_f32_e32 v176, v176, v168
	v_cvt_pk_fp8_f32 v5, v173, v174
	v_cvt_pk_fp8_f32 v5, v175, v176 op_sel:[0,0,1]
	v_permlane32_swap_b32_e32 v2, v3
	s_nop 0
	v_permlane32_swap_b32_e32 v4, v5
	global_store_dwordx4 v[62:63], v[2:5], off offset:800
	s_cbranch_vccz .LBB0_550
	s_waitcnt vmcnt(0)
	s_barrier
	s_and_saveexec_b64 s[4:5], s[0:1]
	s_cbranch_execz .LBB0_549
	s_mov_b64 s[10:11], exec
	v_mbcnt_lo_u32_b32 v2, s10, 0
	buffer_wbl2 sc1
	s_waitcnt vmcnt(0)
	s_waitcnt vmcnt(0)
	v_mbcnt_hi_u32_b32 v2, s11, v2
	v_cmp_eq_u32_e32 vcc, 0, v2
	s_and_b64 s[14:15], exec, vcc
	s_mov_b64 exec, s[14:15]
	s_cbranch_execz .LBB0_549
	s_bcnt1_i32_b64 s10, s[10:11]
	v_mov_b32_e32 v2, s10
	global_atomic_add v0, v2, s[84:85]
	s_branch .LBB0_549
